# speedup vs baseline: 1.0127x; 1.0127x over previous
.LBB0_3:
	s_or_b64 exec, exec, s[6:7]
	v_lshrrev_b32_e32 v26, 3, v0
	v_lshlrev_b32_e32 v41, 2, v26
	s_waitcnt lgkmcnt(0)
	s_barrier
	global_load_dword v34, v41, s[8:9]
	global_load_dword v40, v41, s[10:11]
	v_lshlrev_b32_e32 v19, 3, v0
	v_and_b32_e32 v28, 56, v19
	v_lshlrev_b32_e32 v61, 2, v28
	v_mad_u32_u24 v19, v26, s3, v61
	ds_read2_b32 v[46:47], v19 offset1:1
	ds_read_b128 v[20:23], v61 offset:17664
	ds_read_b128 v[36:39], v61 offset:17680
	ds_read2_b32 v[52:53], v19 offset0:2 offset1:3
	ds_read2_b32 v[58:59], v19 offset0:6 offset1:7
	s_lshl_b32 s6, s18, 21
	s_waitcnt lgkmcnt(3)
	v_pk_add_f32 v[50:51], v[46:47], v[20:21] neg_lo:[0,1] neg_hi:[0,1]
	ds_read_b128 v[46:49], v61 offset:17920
	s_waitcnt lgkmcnt(2)
	v_pk_add_f32 v[52:53], v[52:53], v[22:23] neg_lo:[0,1] neg_hi:[0,1]
	s_lshl_b32 s4, s20, 1
	s_waitcnt lgkmcnt(1)
	v_pk_add_f32 v[58:59], v[58:59], v[38:39] neg_lo:[0,1] neg_hi:[0,1]
	s_add_u32 s4, s12, s4
	s_waitcnt lgkmcnt(0)
	v_pk_mul_f32 v[50:51], v[50:51], v[46:47]
	v_pk_mul_f32 v[52:53], v[52:53], v[48:49]
	s_addc_u32 s5, s13, 0
	v_lshlrev_b32_e32 v32, 1, v28
	v_mov_b32_e32 v33, v31
	v_lshl_add_u64 v[24:25], s[4:5], 0, v[32:33]
	v_mul_u32_u24_e32 v60, 0x104, v26
	v_mov_b32_e32 v27, v31
	s_lshl_b64 s[4:5], s[18:19], 14
	s_or_b64 s[4:5], s[4:5], s[20:21]
	v_add_u32_e32 v1, v30, v1
	ds_read_b128 v[54:57], v61 offset:17936
	s_waitcnt lgkmcnt(0)
	v_pk_mul_f32 v[58:59], v[58:59], v[56:57]
	s_waitcnt vmcnt(0)
	v_pk_fma_f32 v[50:51], v[34:35], v[50:51], v[40:41] op_sel_hi:[0,1,0]
	v_pk_fma_f32 v[52:53], v[34:35], v[52:53], v[40:41] op_sel_hi:[0,1,0]
	v_cvt_pk_f16_f32 v50, v50, v51
	v_cvt_pk_f16_f32 v51, v52, v53
	ds_read2_b32 v[52:53], v19 offset0:4 offset1:5
	s_waitcnt lgkmcnt(0)
	v_pk_add_f32 v[52:53], v[52:53], v[36:37] neg_lo:[0,1] neg_hi:[0,1]
	s_nop 0
	v_pk_mul_f32 v[52:53], v[52:53], v[54:55]
	s_nop 0
	v_pk_fma_f32 v[52:53], v[34:35], v[52:53], v[40:41] op_sel_hi:[0,1,0]
	v_pk_fma_f32 v[34:35], v[34:35], v[58:59], v[40:41] op_sel_hi:[0,1,0]
	v_cvt_pk_f16_f32 v52, v52, v53
	v_cvt_pk_f16_f32 v53, v34, v35
	v_lshl_or_b32 v34, v26, 15, s6
	v_mov_b32_e32 v35, v31
	v_lshl_add_u64 v[34:35], v[24:25], 0, v[34:35]
	global_store_dwordx4 v[34:35], v[50:53], off
	v_lshrrev_b32_e32 v34, 3, v18
	v_lshlrev_b32_e32 v29, 2, v34
	global_load_dword v40, v29, s[8:9]
	global_load_dword v42, v29, s[10:11]
	v_mad_u32_u24 v50, v34, s3, v61
	ds_read2_b32 v[18:19], v50 offset1:1
	v_mov_b32_e32 v35, v31
	s_waitcnt lgkmcnt(0)
	v_pk_add_f32 v[18:19], v[18:19], v[20:21] neg_lo:[0,1] neg_hi:[0,1]
	ds_read2_b32 v[20:21], v50 offset0:2 offset1:3
	v_pk_mul_f32 v[18:19], v[18:19], v[46:47]
	s_waitcnt lgkmcnt(0)
	v_pk_add_f32 v[20:21], v[20:21], v[22:23] neg_lo:[0,1] neg_hi:[0,1]
	s_nop 0
	v_pk_mul_f32 v[20:21], v[20:21], v[48:49]
	ds_read2_b32 v[22:23], v50 offset0:6 offset1:7
	s_waitcnt lgkmcnt(0)
	v_pk_add_f32 v[22:23], v[22:23], v[38:39] neg_lo:[0,1] neg_hi:[0,1]
	ds_read2st64_b32 v[38:39], v41 offset0:69 offset1:70
	v_pk_mul_f32 v[22:23], v[22:23], v[56:57]
	s_waitcnt vmcnt(0)
	v_pk_fma_f32 v[18:19], v[40:41], v[18:19], v[42:43] op_sel_hi:[0,1,0]
	v_pk_fma_f32 v[20:21], v[40:41], v[20:21], v[42:43] op_sel_hi:[0,1,0]
	v_cvt_pk_f16_f32 v18, v18, v19
	v_cvt_pk_f16_f32 v19, v20, v21
	ds_read2_b32 v[20:21], v50 offset0:4 offset1:5
	v_pk_fma_f32 v[22:23], v[40:41], v[22:23], v[42:43] op_sel_hi:[0,1,0]
	s_waitcnt lgkmcnt(0)
	v_pk_add_f32 v[20:21], v[20:21], v[36:37] neg_lo:[0,1] neg_hi:[0,1]
	s_nop 0
	v_pk_mul_f32 v[20:21], v[20:21], v[54:55]
	v_lshl_add_u64 v[36:37], s[14:15], 0, v[32:33]
	v_pk_fma_f32 v[20:21], v[40:41], v[20:21], v[42:43] op_sel_hi:[0,1,0]
	v_cvt_pk_f16_f32 v20, v20, v21
	v_cvt_pk_f16_f32 v21, v22, v23
	v_lshl_or_b32 v22, v34, 15, s6
	v_mov_b32_e32 v23, v31
	v_lshl_add_u64 v[22:23], v[24:25], 0, v[22:23]
	global_store_dwordx4 v[22:23], v[18:21], off
	v_mov_b32_e32 v40, v39
	s_nop 0
	v_lshlrev_b32_e32 v18, 8, v26
	v_sub_u32_e32 v41, v60, v18
	v_mad_u32_u24 v31, v28, s3, v41
	ds_read2_b32 v[18:19], v31 offset1:65
	v_lshl_add_u64 v[26:27], s[4:5], 0, v[26:27]
	s_waitcnt lgkmcnt(0)
	v_pk_add_f32 v[18:19], v[18:19], v[38:39] op_sel_hi:[1,0] neg_lo:[0,1] neg_hi:[0,1]
	s_nop 0
	v_pk_mul_f32 v[46:47], v[40:41], v[18:19] op_sel_hi:[0,1]
	global_load_dwordx4 v[18:21], v61, s[8:9] offset:16
	global_load_dwordx4 v[52:55], v61, s[8:9]
	global_load_dwordx4 v[22:25], v61, s[10:11] offset:16
	global_load_dwordx4 v[56:59], v61, s[10:11]
	v_mov_b32_e32 v39, 0x208
	v_mad_u32_u24 v64, v28, s3, v39
	s_waitcnt vmcnt(0)
	v_pk_fma_f32 v[46:47], v[52:53], v[46:47], v[56:57]
	s_nop 0
	v_cvt_pk_f16_f32 v60, v46, v47
	v_add_u32_e32 v47, 0x200, v31
	v_add_u32_e32 v46, v41, v64
	ds_read2_b32 v[50:51], v47 offset0:67 offset1:197
	ds_read_b32 v48, v46
	s_waitcnt lgkmcnt(1)
	v_mov_b32_e32 v49, v50
	s_waitcnt lgkmcnt(0)
	v_pk_add_f32 v[48:49], v[48:49], v[38:39] op_sel_hi:[1,0] neg_lo:[0,1] neg_hi:[0,1]
	v_mov_b32_e32 v39, 0x410
	v_pk_mul_f32 v[48:49], v[40:41], v[48:49] op_sel_hi:[0,1]
	v_pk_fma_f32 v[48:49], v[54:55], v[48:49], v[58:59]
	v_mad_u32_u24 v65, v28, s3, v39
	v_cvt_pk_f16_f32 v61, v48, v49
	v_add_u32_e32 v48, v41, v65
	ds_read_b32 v50, v48
	s_waitcnt lgkmcnt(0)
	v_pk_add_f32 v[50:51], v[50:51], v[38:39] op_sel_hi:[1,0] neg_lo:[0,1] neg_hi:[0,1]
	v_mov_b32_e32 v39, 0x618
	v_pk_mul_f32 v[50:51], v[40:41], v[50:51] op_sel_hi:[0,1]
	v_mad_u32_u24 v66, v28, s3, v39
	v_pk_fma_f32 v[50:51], v[18:19], v[50:51], v[22:23]
	v_add_u32_e32 v49, v41, v66
	v_cvt_pk_f16_f32 v62, v50, v51
	ds_read_b32 v50, v49
	ds_read_b32 v51, v31 offset:1820
	s_waitcnt lgkmcnt(0)
	v_pk_add_f32 v[38:39], v[50:51], v[38:39] op_sel_hi:[1,0] neg_lo:[0,1] neg_hi:[0,1]
	s_nop 0
	v_pk_mul_f32 v[38:39], v[40:41], v[38:39] op_sel_hi:[0,1]
	v_pk_fma_f32 v[38:39], v[20:21], v[38:39], v[24:25]
	v_mad_u32_u24 v50, v28, s3, v29
	v_cvt_pk_f16_f32 v63, v38, v39
	v_lshlrev_b64 v[38:39], 7, v[26:27]
	v_lshl_add_u64 v[26:27], v[36:37], 0, v[38:39]
	global_store_dwordx4 v[26:27], v[60:63], off sc1
	ds_read2st64_b32 v[40:41], v29 offset0:69 offset1:70
	ds_read2_b32 v[26:27], v50 offset1:65
	v_add_u32_e32 v51, 0x200, v50
	s_waitcnt lgkmcnt(1)
	v_mov_b32_e32 v42, v41
	s_waitcnt lgkmcnt(0)
	v_pk_add_f32 v[26:27], v[26:27], v[40:41] op_sel_hi:[1,0] neg_lo:[0,1] neg_hi:[0,1]
	v_add_u32_e32 v41, v29, v64
	v_pk_mul_f32 v[26:27], v[42:43], v[26:27] op_sel_hi:[0,1]
	v_pk_fma_f32 v[26:27], v[52:53], v[26:27], v[56:57]
	ds_read2_b32 v[56:57], v51 offset0:67 offset1:197
	ds_read_b32 v52, v41
	v_cvt_pk_f16_f32 v26, v26, v27
	s_waitcnt lgkmcnt(1)
	v_mov_b32_e32 v53, v56
	s_waitcnt lgkmcnt(0)
	v_pk_add_f32 v[52:53], v[52:53], v[40:41] op_sel_hi:[1,0] neg_lo:[0,1] neg_hi:[0,1]
	s_nop 0
	v_pk_mul_f32 v[52:53], v[42:43], v[52:53] op_sel_hi:[0,1]
	v_pk_fma_f32 v[52:53], v[54:55], v[52:53], v[58:59]
	v_add_u32_e32 v54, v29, v65
	ds_read_b32 v56, v54
	v_cvt_pk_f16_f32 v27, v52, v53
	s_waitcnt lgkmcnt(0)
	v_pk_add_f32 v[52:53], v[56:57], v[40:41] op_sel_hi:[1,0] neg_lo:[0,1] neg_hi:[0,1]
	s_nop 0
	v_pk_mul_f32 v[52:53], v[42:43], v[52:53] op_sel_hi:[0,1]
	v_pk_fma_f32 v[18:19], v[18:19], v[52:53], v[22:23]
	v_add_u32_e32 v22, v29, v66
	v_cvt_pk_f16_f32 v28, v18, v19
	ds_read_b32 v18, v22
	ds_read_b32 v19, v50 offset:1820
	s_waitcnt lgkmcnt(0)
	v_pk_add_f32 v[18:19], v[18:19], v[40:41] op_sel_hi:[1,0] neg_lo:[0,1] neg_hi:[0,1]
	s_nop 0
	v_pk_mul_f32 v[18:19], v[42:43], v[18:19] op_sel_hi:[0,1]
	v_pk_fma_f32 v[18:19], v[20:21], v[18:19], v[24:25]
	s_nop 0
	v_cvt_pk_f16_f32 v29, v18, v19
	v_lshl_add_u64 v[18:19], s[4:5], 0, v[34:35]
	v_lshlrev_b64 v[18:19], 7, v[18:19]
	v_lshl_add_u64 v[20:21], v[36:37], 0, v[18:19]
	global_store_dwordx4 v[20:21], v[26:29], off sc1
	v_cmp_gt_u32_e32 vcc, 0x80, v0
	s_and_saveexec_b64 s[6:7], vcc
	s_cbranch_execz .Lk0_hskip
	v_lshrrev_b32_e32 v56, 5, v0
	v_bfe_u32 v57, v0, 4, 1
	v_lshlrev_b32_e32 v56, 4, v56
	v_mad_u32_u24 v56, v57, 15, v56
	v_and_b32_e32 v57, 15, v0
	v_mul_u32_u24_e32 v57, 0x410, v57
	v_lshl_add_u32 v56, v56, 2, v57
	ds_read2_b32 v[58:59], v56 offset1:65
	ds_read2_b32 v[60:61], v56 offset0:130 offset1:195
	s_lshl_b32 s4, s2, 11
	s_add_u32 s4, s12, s4
	s_addc_u32 s5, s13, 0
	s_add_u32 s4, s4, 0x2000000
	s_addc_u32 s5, s5, 0
	v_lshlrev_b32_e32 v62, 4, v0
	s_waitcnt lgkmcnt(0)
	global_store_dwordx4 v62, v[58:61], s[4:5] sc1
.Lk0_hskip:
	s_or_b64 exec, exec, s[6:7]
	s_barrier
	ds_write2_b32 v1, v14, v15 offset1:1
	ds_write2_b32 v1, v16, v17 offset0:2 offset1:3
	v_add_u32_e32 v1, v30, v44
	ds_write2_b32 v1, v10, v11 offset1:1
	ds_write2_b32 v1, v12, v13 offset0:2 offset1:3
	v_add_u32_e32 v1, v30, v43
	ds_write2_b32 v1, v6, v7 offset1:1
	ds_write2_b32 v1, v8, v9 offset0:2 offset1:3
	v_add_u32_e32 v1, v30, v45
	ds_write2_b32 v1, v2, v3 offset1:1
	ds_write2_b32 v1, v4, v5 offset0:2 offset1:3
	s_waitcnt lgkmcnt(0)
	s_barrier
	ds_read2_b32 v[8:9], v31 offset1:65
	ds_read_b32 v1, v46
	ds_read2_b32 v[2:3], v47 offset0:67 offset1:197
	ds_read_b32 v4, v48
	ds_read_b32 v5, v49
	ds_read_b32 v10, v31 offset:1820
	v_lshl_add_u64 v[6:7], s[16:17], 0, v[32:33]
	s_mov_b64 s[4:5], 0
	s_waitcnt lgkmcnt(2)
	v_cvt_pk_f16_f32 v4, v4, v3
	v_cvt_pk_f16_f32 v3, v1, v2
	s_waitcnt lgkmcnt(0)
	v_cvt_pk_f16_f32 v5, v5, v10
	v_cvt_pk_f16_f32 v2, v8, v9
	v_lshl_add_u64 v[8:9], v[6:7], 0, v[38:39]
	global_store_dwordx4 v[8:9], v[2:5], off sc1
	ds_read2_b32 v[8:9], v50 offset1:65
	ds_read_b32 v1, v41
	ds_read2_b32 v[2:3], v51 offset0:67 offset1:197
	ds_read_b32 v4, v54
	ds_read_b32 v5, v22
	ds_read_b32 v10, v50 offset:1820
	v_lshl_add_u64 v[6:7], v[6:7], 0, v[18:19]
	s_waitcnt lgkmcnt(2)
	v_cvt_pk_f16_f32 v4, v4, v3
	v_cvt_pk_f16_f32 v3, v1, v2
	s_waitcnt lgkmcnt(0)
	v_cvt_pk_f16_f32 v5, v5, v10
	v_cvt_pk_f16_f32 v2, v8, v9
	global_store_dwordx4 v[6:7], v[2:5], off sc1

.LBB4_30:
	s_andn2_saveexec_b64 s[6:7], s[8:9]
	v_add_u32_e32 v22, 1, v98
	s_or_b64 exec, exec, s[6:7]
	v_mov_b32_e32 v23, 57
	v_mul_lo_u16_sdwa v23, v22, v23 dst_sel:DWORD dst_unused:UNUSED_PAD src0_sel:BYTE_0 src1_sel:DWORD
	v_lshrrev_b16_e32 v23, 10, v23
	v_mul_i32_i24_e32 v24, 0xffffffee, v23
	v_add_u32_e32 v23, s26, v23
	v_add3_u32 v24, s28, v22, v24
	s_movk_i32 s6, 0xb4
	v_cmp_gt_u32_e64 s[6:7], s6, v22
	v_or_b32_e32 v22, v24, v23
	s_movk_i32 s8, 0x80
	v_cmp_gt_u32_e64 s[8:9], s8, v22
	v_mov_b32_e32 v22, 0x7f
	v_med3_i32 v76, v23, 0, v22
	v_med3_i32 v78, v24, 0, v22
	v_ashrrev_i32_e32 v86, 4, v24
	v_and_b32_e32 v87, 15, v24
	v_cmp_eq_u32_e64 s[100:101], 15, v87
	v_lshlrev_b32_e32 v86, 1, v86
	s_nop 0
	v_cndmask_b32_e64 v87, 0, 1, s[100:101]
	v_or_b32_e32 v86, v86, v87
	v_med3_i32 v86, v86, 0, 15
	v_lshl_add_u32 v86, v76, 4, v86
	v_readfirstlane_b32 s33, v1
	s_lshr_b32 s100, s18, 3
	v_add_u32_e32 v86, s100, v86
	v_lshlrev_b32_e32 v86, 8, v86
	v_lshl_add_u32 v86, v73, 4, v86
	v_lshlrev_b32_e32 v22, 7, v76
	v_or3_b32 v22, s18, v22, v78
	v_mov_b32_e32 v23, s19
	v_lshlrev_b64 v[26:27], 7, v[22:23]
	v_lshl_add_u64 v[22:23], s[14:15], 0, v[26:27]
	v_lshlrev_b32_e32 v38, 1, v103
	v_mov_b32_e32 v39, 0
	v_lshl_add_u64 v[26:27], s[10:11], 0, v[26:27]
	v_lshl_add_u64 v[22:23], v[22:23], 0, v[38:39]
	v_lshl_add_u64 v[26:27], v[26:27], 0, v[38:39]
	global_load_dwordx4 v[30:33], v[22:23], off
	s_nop 0
	global_load_dwordx4 v[22:25], v[22:23], off offset:64
	s_nop 0
	global_load_dwordx4 v[34:37], v[26:27], off
	s_nop 0
	global_load_dwordx4 v[26:29], v[26:27], off offset:64
	s_cmp_lt_u32 s33, 2
	s_cbranch_scc1 .Lk4h_rows
	s_add_u32 s100, s14, 0xff800000
	s_addc_u32 s101, s15, -1
	s_and_b64 s[6:7], s[6:7], s[8:9]
	v_mov_b32_e32 v38, v39
	global_load_dwordx4 v[76:79], v86, s[100:101] offset:192
	global_load_dwordx4 v[82:85], v86, s[100:101] offset:64
	global_load_dwordx4 v[90:93], v86, s[100:101]
	global_load_dwordx4 v[86:89], v86, s[100:101] offset:128
	s_waitcnt vmcnt(0)
	v_mov_b32_e32 v80, v79
	v_mov_b32_e32 v79, v86
	v_mov_b32_e32 v86, v87
	v_mov_b32_e32 v87, v88
	v_mov_b32_e32 v88, v89
	v_mov_b32_e32 v89, v76
	v_mov_b32_e32 v76, v92
	v_mov_b32_e32 v92, v90
	v_mov_b32_e32 v90, v77
	v_mov_b32_e32 v77, v93
	v_mov_b32_e32 v93, v91
	v_mov_b32_e32 v91, v78
	s_branch .Lk4h_join
.Lk4h_rows:
	v_lshlrev_b32_e32 v38, 9, v76
	v_lshl_add_u64 v[76:77], s[12:13], 0, v[38:39]
	v_lshlrev_b32_e32 v38, 2, v78
	v_lshl_add_u64 v[80:81], v[76:77], 0, v[38:39]
	v_lshl_add_u64 v[76:77], v[80:81], 0, v[40:41]
	v_lshl_add_u64 v[86:87], v[80:81], 0, v[58:59]
	global_load_dword v92, v[76:77], off
	v_lshl_add_u64 v[88:89], v[80:81], 0, v[60:61]
	global_load_dword v86, v[86:87], off
	v_lshl_add_u64 v[76:77], v[80:81], 0, v[42:43]
	global_load_dword v93, v[76:77], off
	global_load_dword v87, v[88:89], off
	v_lshl_add_u64 v[76:77], v[80:81], 0, v[44:45]
	v_lshl_add_u64 v[78:79], v[80:81], 0, v[46:47]
	v_lshl_add_u64 v[88:89], v[80:81], 0, v[62:63]
	v_lshl_add_u64 v[90:91], v[80:81], 0, v[64:65]
	global_load_dword v76, v[76:77], off
	v_lshl_add_u64 v[94:95], v[80:81], 0, v[68:69]
	global_load_dword v88, v[88:89], off
	s_and_b64 s[6:7], s[6:7], s[8:9]
	global_load_dword v77, v[78:79], off
	global_load_dword v89, v[90:91], off
	v_lshl_add_u64 v[78:79], v[80:81], 0, v[48:49]
	v_lshl_add_u64 v[90:91], v[80:81], 0, v[66:67]
	global_load_dword v82, v[78:79], off
	v_mov_b32_e32 v38, v39
	global_load_dword v90, v[90:91], off
	v_lshl_add_u64 v[78:79], v[80:81], 0, v[50:51]
	global_load_dword v83, v[78:79], off
	global_load_dword v91, v[94:95], off
	v_lshl_add_u64 v[78:79], v[80:81], 0, v[52:53]
	global_load_dword v84, v[78:79], off
	v_lshl_add_u64 v[78:79], v[80:81], 0, v[54:55]
	global_load_dword v85, v[78:79], off
	v_lshl_add_u64 v[78:79], v[80:81], 0, v[56:57]
	v_lshl_add_u64 v[80:81], v[80:81], 0, v[70:71]
	global_load_dword v79, v[78:79], off
	s_nop 0
	global_load_dword v80, v[80:81], off
.Lk4h_join:
	ds_read_b128 v[94:97], v102
	ds_read_b128 v[110:113], v102 offset:4096
	s_waitcnt vmcnt(19) lgkmcnt(1)
	v_mfma_f32_16x16x32_f16 v[94:97], v[94:97], v[30:33], 0
	s_waitcnt vmcnt(17) lgkmcnt(0)
	v_mfma_f32_16x16x32_f16 v[110:113], v[110:113], v[34:37], 0
	s_nop 7
	v_pk_mul_f32 v[96:97], v[96:97], v[112:113]
	v_pk_mul_f32 v[94:95], v[94:95], v[110:111]
	ds_read_b128 v[110:113], v102 offset:1024
	ds_read_b128 v[114:117], v102 offset:5120
	s_waitcnt lgkmcnt(1)
	v_mfma_f32_16x16x32_f16 v[30:33], v[110:113], v[30:33], 0
	s_waitcnt lgkmcnt(0)
	v_mfma_f32_16x16x32_f16 v[34:37], v[114:117], v[34:37], 0
	s_nop 7
	v_pk_mul_f32 v[110:111], v[32:33], v[36:37]
	v_pk_mul_f32 v[112:113], v[30:31], v[34:35]
	ds_read_b128 v[30:33], v102 offset:2048
	ds_read_b128 v[34:37], v102 offset:6144
	s_waitcnt lgkmcnt(1)
	v_mfma_f32_16x16x32_f16 v[30:33], v[30:33], v[22:25], 0
	s_waitcnt vmcnt(16) lgkmcnt(0)
	v_mfma_f32_16x16x32_f16 v[34:37], v[34:37], v[26:29], 0
	s_nop 7
	v_pk_mul_f32 v[114:115], v[32:33], v[36:37]
	v_pk_mul_f32 v[116:117], v[30:31], v[34:35]
	ds_read_b128 v[30:33], v102 offset:3072
	ds_read_b128 v[34:37], v102 offset:7168
	s_waitcnt lgkmcnt(1)
	v_mfma_f32_16x16x32_f16 v[22:25], v[30:33], v[22:25], 0
	s_waitcnt lgkmcnt(0)
	v_mfma_f32_16x16x32_f16 v[26:29], v[34:37], v[26:29], 0
	s_nop 7
	v_pk_mul_f32 v[24:25], v[24:25], v[28:29]
	v_pk_mul_f32 v[30:31], v[22:23], v[26:27]
	v_cvt_pk_f16_f32 v25, v24, v25
	v_cvt_pk_f16_f32 v24, v30, v31
	ds_read_b128 v[30:33], v102 offset:8192
	ds_read_b128 v[34:37], v102 offset:9216
	v_cvt_pk_f16_f32 v29, v110, v111
	v_cvt_pk_f16_f32 v27, v96, v97
	v_cvt_pk_f16_f32 v28, v112, v113
	v_cvt_pk_f16_f32 v26, v94, v95
	v_cvt_pk_f16_f32 v23, v114, v115
	v_cvt_pk_f16_f32 v22, v116, v117
	s_waitcnt lgkmcnt(1)
	v_mfma_f32_16x16x32_f16 v[30:33], v[30:33], v[26:29], 0
	s_waitcnt lgkmcnt(0)
	v_mfma_f32_16x16x32_f16 v[30:33], v[34:37], v[22:25], v[30:33]
	s_waitcnt vmcnt(13)
	s_nop 6
	v_pk_add_f32 v[34:35], v[92:93], v[30:31]
	ds_read_b128 v[92:95], v102 offset:10240
	ds_read_b128 v[110:113], v102 offset:11264
	s_waitcnt lgkmcnt(1)
	v_mfma_f32_16x16x32_f16 v[92:95], v[92:95], v[26:29], 0
	v_add_f32_e32 v30, 0, v34
	v_add_f32_e32 v30, v35, v30
	s_waitcnt vmcnt(9)
	v_pk_add_f32 v[32:33], v[76:77], v[32:33]
	s_waitcnt lgkmcnt(0)
	v_mfma_f32_16x16x32_f16 v[92:95], v[110:113], v[22:25], v[92:95]
	ds_read_b128 v[110:113], v102 offset:12288
	ds_read_b128 v[114:117], v102 offset:13312
	s_waitcnt lgkmcnt(1)
	v_mfma_f32_16x16x32_f16 v[110:113], v[110:113], v[26:29], 0
	s_waitcnt vmcnt(5)
	s_nop 2
	v_pk_add_f32 v[82:83], v[82:83], v[92:93]
	s_waitcnt vmcnt(2)
	v_pk_add_f32 v[84:85], v[84:85], v[94:95]
	s_waitcnt lgkmcnt(0)
	v_mfma_f32_16x16x32_f16 v[110:113], v[114:117], v[22:25], v[110:113]
	ds_read_b128 v[114:117], v102 offset:14336
	ds_read_b128 v[118:121], v102 offset:15360
	s_waitcnt lgkmcnt(1)
	v_mfma_f32_16x16x32_f16 v[26:29], v[114:117], v[26:29], 0
	s_waitcnt lgkmcnt(0)
	v_mfma_f32_16x16x32_f16 v[22:25], v[118:121], v[22:25], v[26:29]
	s_nop 5
	v_mov_b32_e32 v28, v111
	v_mov_b32_e32 v29, v112
	v_mov_b32_e32 v27, v24
	v_add_f32_e32 v24, v32, v30
	v_add_f32_e32 v24, v33, v24
	v_add_f32_e32 v24, v24, v82
	v_add_f32_e32 v24, v83, v24
	v_add_f32_e32 v78, v84, v24
	v_pk_mov_b32 v[30:31], v[84:85], v[110:111] op_sel:[1,0]
	v_pk_add_f32 v[28:29], v[86:87], v[28:29]
	s_waitcnt vmcnt(1)
	v_pk_add_f32 v[36:37], v[30:31], v[78:79]
	v_mov_b32_e32 v26, v23
	v_pk_add_f32 v[30:31], v[36:37], v[36:37] op_sel:[0,1] op_sel_hi:[1,0]
	v_pk_mov_b32 v[22:23], v[112:113], v[22:23] op_sel:[1,0]
	v_pk_add_f32 v[30:31], v[28:29], v[30:31]
	v_pk_add_f32 v[22:23], v[88:89], v[22:23]
	v_pk_add_f32 v[30:31], v[28:29], v[30:31] op_sel:[1,0] op_sel_hi:[0,1]
	v_pk_add_f32 v[30:31], v[22:23], v[30:31]
	v_pk_add_f32 v[26:27], v[90:91], v[26:27]
	v_pk_add_f32 v[30:31], v[30:31], v[22:23] op_sel:[0,1] op_sel_hi:[1,0]
	v_mov_b32_e32 v24, v25
	v_pk_add_f32 v[30:31], v[26:27], v[30:31]
	v_mov_b32_e32 v25, v27
	v_mov_b32_e32 v81, v30
	s_waitcnt vmcnt(0)
	v_pk_add_f32 v[30:31], v[80:81], v[24:25]
	v_mov_b32_e32 v91, v39
	v_add_f32_e32 v24, v30, v31
	ds_bpermute_b32 v25, v108, v24
	v_mov_b32_e32 v90, v39
	v_mov_b32_e32 v88, v39
	v_mov_b32_e32 v89, v39
	s_waitcnt lgkmcnt(0)
	v_add_f32_e32 v24, v24, v25
	ds_bpermute_b32 v25, v109, v24
	s_waitcnt lgkmcnt(0)
	v_add_f32_e32 v25, v24, v25
	v_mul_f32_e32 v24, 0x3c800000, v25
	v_fmac_f32_e32 v35, 0xbc800000, v25
	v_fmamk_f32 v36, v25, 0xbc800000, v34
	v_mul_f32_e32 v31, v35, v35
	v_pk_add_f32 v[76:77], v[32:33], v[24:25] op_sel_hi:[1,0] neg_lo:[0,1] neg_hi:[0,1]
	v_fmac_f32_e32 v31, v36, v36
	v_pk_mul_f32 v[32:33], v[76:77], v[76:77]
	v_pk_add_f32 v[78:79], v[82:83], v[24:25] op_sel_hi:[1,0] neg_lo:[0,1] neg_hi:[0,1]
	v_add_f32_e32 v31, v32, v31
	v_add_f32_e32 v31, v33, v31
	v_pk_mul_f32 v[32:33], v[78:79], v[78:79]
	v_pk_add_f32 v[80:81], v[84:85], v[24:25] op_sel_hi:[1,0] neg_lo:[0,1] neg_hi:[0,1]
	v_add_f32_e32 v31, v32, v31
	v_add_f32_e32 v31, v33, v31
	v_pk_mul_f32 v[32:33], v[80:81], v[80:81]
	v_fmac_f32_e32 v37, 0xbc800000, v25
	v_add_f32_e32 v31, v32, v31
	v_add_f32_e32 v31, v33, v31
	v_pk_add_f32 v[82:83], v[28:29], v[24:25] op_sel_hi:[1,0] neg_lo:[0,1] neg_hi:[0,1]
	v_fmac_f32_e32 v31, v37, v37
	v_pk_mul_f32 v[28:29], v[82:83], v[82:83]
	v_pk_add_f32 v[84:85], v[22:23], v[24:25] op_sel_hi:[1,0] neg_lo:[0,1] neg_hi:[0,1]
	v_add_f32_e32 v28, v28, v31
	v_add_f32_e32 v28, v29, v28
	v_pk_mul_f32 v[22:23], v[84:85], v[84:85]
	v_pk_add_f32 v[86:87], v[26:27], v[24:25] op_sel_hi:[1,0] neg_lo:[0,1] neg_hi:[0,1]
	v_add_f32_e32 v22, v22, v28
	v_add_f32_e32 v28, v23, v22
	v_pk_mul_f32 v[22:23], v[86:87], v[86:87]
	v_fmac_f32_e32 v30, 0xbc800000, v25
	v_add_f32_e32 v22, v22, v28
	v_add_f32_e32 v22, v23, v22
	v_fmac_f32_e32 v22, v30, v30
	ds_bpermute_b32 v23, v108, v22
	v_mov_b32_e32 v33, v39
	v_mov_b32_e32 v32, v39
	v_mov_b32_e32 v31, v39
	s_waitcnt lgkmcnt(0)
	v_add_f32_e32 v22, v22, v23
	ds_bpermute_b32 v23, v109, v22
	s_waitcnt lgkmcnt(0)
	v_add_f32_e32 v22, v22, v23
	v_mov_b32_e32 v23, 0x3727c5ac
	v_fmac_f32_e32 v23, 0x3c800000, v22
	v_rsq_f32_e32 v34, v23
	ds_read_b128 v[22:25], v107 offset:16384
	ds_read_b128 v[26:29], v107 offset:16640
	s_and_saveexec_b64 s[8:9], s[6:7]
	s_cbranch_execz .LBB4_34
	ds_read_b128 v[90:93], v107 offset:16576
	ds_read_b128 v[94:97], v107 offset:16832
	ds_read_b128 v[108:111], v107 offset:16704
	ds_read_b128 v[112:115], v107 offset:16768
	ds_read_b128 v[116:119], v107 offset:16512
	v_pk_mul_f32 v[32:33], v[86:87], v[34:35] op_sel_hi:[1,0]
	s_waitcnt lgkmcnt(4)
	v_mov_b32_e32 v38, v91
	v_mov_b32_e32 v39, v92
	s_waitcnt lgkmcnt(3)
	v_mov_b32_e32 v86, v95
	v_mov_b32_e32 v87, v96
	v_pk_fma_f32 v[32:33], v[32:33], v[38:39], v[86:87]
	v_pk_mul_f32 v[76:77], v[76:77], v[34:35] op_sel_hi:[1,0]
	v_cvt_pk_f16_f32 v38, v32, v33
	v_pk_mul_f32 v[32:33], v[84:85], v[34:35] op_sel_hi:[1,0]
	ds_read_b128 v[84:87], v107 offset:16448
	s_waitcnt lgkmcnt(1)
	v_pk_mov_b32 v[88:89], v[118:119], v[90:91] op_sel:[1,0]
	v_pk_mov_b32 v[90:91], v[114:115], v[94:95] op_sel:[1,0]
	v_mul_f32_e32 v31, v37, v34
	v_pk_fma_f32 v[32:33], v[32:33], v[88:89], v[90:91]
	v_mov_b32_e32 v90, v113
	v_cvt_pk_f16_f32 v88, v32, v33
	v_pk_mul_f32 v[32:33], v[82:83], v[34:35] op_sel_hi:[1,0]
	v_mov_b32_e32 v82, v117
	v_mov_b32_e32 v83, v118
	v_mov_b32_e32 v91, v114
	v_pk_fma_f32 v[32:33], v[32:33], v[82:83], v[90:91]
	v_pk_fma_f32 v[24:25], v[24:25], v[76:77], v[28:29]
	v_cvt_pk_f16_f32 v89, v32, v33
	v_fma_mixlo_f16 v39, v31, v116, v112
	v_pk_mul_f32 v[32:33], v[80:81], v[34:35] op_sel_hi:[1,0]
	v_pk_mul_f32 v[78:79], v[78:79], v[34:35] op_sel_hi:[1,0]
	v_cvt_pk_f16_f32 v31, v24, v25
	v_mul_f32_e32 v24, v35, v34
	s_waitcnt lgkmcnt(0)
	v_pk_fma_f32 v[32:33], v[32:33], v[86:87], v[110:111]
	v_pk_fma_f32 v[78:79], v[78:79], v[84:85], v[108:109]
	v_fma_mixlo_f16 v91, v23, v24, v27
	v_mul_f32_e32 v23, v30, v34
	v_cvt_pk_f16_f32 v33, v32, v33
	v_cvt_pk_f16_f32 v32, v78, v79
	v_fma_mixlo_f16 v90, v23, v93, v97
